# NA unit: bias-table fill issues its four table loads together (one wait instead of four dependent round trips); MLA unit prologue wait leaves the just-issued LDS-DMA pieces in flight
# speedup vs baseline: 1.0267x; 1.0267x over previous
; DEV void na_unit(const Params& p, int layer, int b, int hd, int rg, bool ctxq, LAS char* lds) {
;     ...
;         const int R = rg * 4; T0 = min(max(R - 4, 0), 248); const int T1 = min(max(R + 3 - 4, 0), 248) + 7; ntl = T1 - T0 + 1; my0 = min(max(qrow - 4, 0), 248);
;         wlo = min(max(rp - 4, 0), 248); whi = min(max(rp + 1 - 4, 0), 248) + 8; ks0 = min(max(16 * cb - 8, 0), 32);
;         for (int i = tid; i < 15 * 128; i += 512) { const int dr = i >> 7, d = (i & 127) - 64; tb[i] = (d >= -15 && d <= 15) ? p.b_rpb[((layer * 6 + hd) * 15 + dr) * 31 + d + 15] * LOG2E : -1e30f; }
.LBB0_666:
	v_mov_b32_e32 v5, 0xf149f2ca
	v_mov_b32_e32 v8, 0xf149f2ca
	v_mov_b32_e32 v9, 0xf149f2ca
	v_mov_b32_e32 v10, 0xf149f2ca
	s_movk_i32 s2, 0x180
	v_cmp_gt_u32_e64 s[20:21], s2, v4
	s_and_saveexec_b64 s[40:41], vcc
	s_cbranch_execz .Lna_tb_fill
	v_ashrrev_i32_e32 v6, 7, v4
	v_add_u32_e32 v6, s19, v6
	v_mul_lo_u32 v6, v6, 31
	v_ashrrev_i32_e32 v7, 31, v6
	v_lshl_add_u64 v[6:7], v[178:179], 0, v[6:7]
	v_lshl_add_u64 v[6:7], v[6:7], 2, s[72:73]
	global_load_dword v5, v[6:7], off offset:-196
	global_load_dword v8, v[6:7], off offset:300
	global_load_dword v9, v[6:7], off offset:796
	s_and_b64 exec, exec, s[20:21]
	global_load_dword v10, v[6:7], off offset:1292
	s_and_b64 exec, s[40:41], vcc
	s_waitcnt vmcnt(0)
	v_mul_f32_e32 v5, 0x3fb8aa3b, v5
	v_mul_f32_e32 v8, 0x3fb8aa3b, v8
	v_mul_f32_e32 v9, 0x3fb8aa3b, v9
	v_mul_f32_e32 v10, 0x3fb8aa3b, v10
.Lna_tb_fill:
	s_or_b64 exec, exec, s[40:41]
	ds_write_b32 v2, v5
	ds_write_b32 v2, v8 offset:2048
	ds_write_b32 v2, v9 offset:4096
	s_and_b64 exec, exec, s[20:21]
	ds_write_b32 v2, v10 offset:6144

; #define WAITV(n) asm volatile("s_waitcnt vmcnt(%0)" ::"n"(n) : "memory")
; #define SBAR() do { asm volatile("s_waitcnt lgkmcnt(0)" ::: "memory"); __builtin_amdgcn_s_barrier(); asm volatile("" ::: "memory"); } while (0)
; DEV int otid() { int t = threadIdx.x; asm volatile("" : "+v"(t)); return t; }
; DEV unsigned char* ows_(unsigned char* w) { gptr_t g = (gptr_t)w; asm volatile("" : "+s"(g)); return (unsigned char*)g; }
; DEV unsigned lds_addr(LAS char* p) { return (unsigned)(uintptr_t)p; }
; #define MLA_ISSUE(t_, st_) do { const unsigned char* s_ = imgs + (size_t)(t_) * MLA_IMG + wid * (STG / 8) + lane * 16; const unsigned d_ = ldsw + (unsigned)((st_) * STG); \
;     _Pragma("unroll") for (int i_ = 0; i_ < STG / 8192; ++i_) glds16a(s_ + i_ * 1024, d_ + i_ * 1024); } while (0)
; template <int VAR> DEV void mla_unit(const Params& p, int layer, int b, int hd, int tokbase, int t0, int t1, LAS char* lds, SideJob& sj) {
;     unsigned char* ws = ows_(p.ws); const int tid = otid(), lane = tid & 63, wid = tid >> 6, r = lane & 31, h = lane >> 5;
;     constexpr int STG = MLA_IMG;
;     const float cinit = 15.0f - ((const float*)(ws + WS_SCAL))[layer * 8 + 1];
;     const int tok = tokbase + 32 * wid + r;
;     v8i qf[2];
; #pragma unroll
;     for (int sx = 0; sx < 2; ++sx) { const u32x4* q8 = (const u32x4*)(ws + WS_QC + (size_t)tok * 768 + hd * 128 + 64 * sx + 32 * h); const u32x4 a = q8[0], bq = q8[1];
;         qf[sx] = (v8i){(int)a[0], (int)a[1], (int)a[2], (int)a[3], (int)bq[0], (int)bq[1], (int)bq[2], (int)bq[3]}; }
;     const unsigned char* imgs = ws + WS_KVC + (size_t)((b * 6 + hd) * 130) * MLA_IMG;
;     const unsigned ldsw = (unsigned)__builtin_amdgcn_readfirstlane((int)(lds_addr(lds) + (unsigned)(wid * (STG / 8))));
;     ...
;     f32x16 cini, sA0, sA1, sB0, sB1, o0, o1, lacc;
; #pragma unroll
;     for (int i = 0; i < 16; ++i) { cini[i] = cinit; o0[i] = 0.f; o1[i] = 0.f; lacc[i] = 0.f; }
;     const unsigned koffl = (unsigned)(2 * h * 1024 + r * 16);
;     const unsigned voffl = (unsigned)MLA_VOFF + (unsigned)(2 * h * 1024 + r * 16);
;     const int ns = t1 - t0;
;     MLA_ISSUE(t0, 0);
;     WAITV(0); SBAR();
.LBB0_808:
	s_and_b64 vcc, exec, s[6:7]
	s_cbranch_vccz .LBB0_749
	s_ashr_i32 s2, s64, 6
	s_mul_hi_i32 s3, s2, 0x2aaaaaab
	s_lshr_b32 s6, s3, 31
	s_add_i32 s3, s3, s6
	s_mul_i32 s6, s3, 6
	s_sub_i32 s37, s2, s6
	s_lshl_b32 s6, s64, 8
	s_lshl_b32 s3, s3, 14
	s_and_b32 s6, s6, 0x3f00
	s_or_b32 s3, s3, s6
	s_mov_b64 s[6:7], s[38:39]
	v_mov_b32_e32 v52, v246
	s_lshl_b64 s[8:9], s[48:49], 2
	v_and_b32_e32 v7, 31, v52
	v_ashrrev_i32_e32 v6, 6, v52
	s_add_u32 s8, s6, s8
	v_or_b32_e32 v2, s3, v7
	s_addc_u32 s9, s7, s9
	v_lshl_add_u32 v180, v6, 5, v2
	v_mov_b64_e32 v[2:3], s[6:7]
	s_movk_i32 s3, 0x300
	global_load_dword v8, v247, s[8:9] offset:4
	v_mad_i64_i32 v[2:3], s[8:9], v180, s3, v[2:3]
	s_lshl_b32 s8, s37, 7
	s_ashr_i32 s9, s8, 31
	v_lshl_add_u64 v[2:3], v[2:3], 0, s[8:9]
	v_and_b32_e32 v178, 32, v52
	v_lshl_add_u64 v[2:3], v[2:3], 0, v[178:179]
	s_mov_b64 s[8:9], 0x33370100
	s_mov_b32 s3, 0x33370000
	v_lshl_add_u64 v[4:5], v[2:3], 0, s[8:9]
	v_add_co_u32_e32 v2, vcc, s3, v2
	s_mul_i32 s3, s2, 0x82
	s_nop 0
	v_addc_co_u32_e32 v3, vcc, 0, v3, vcc
	global_load_dwordx4 v[138:141], v[2:3], off offset:256
	global_load_dwordx4 v[142:145], v[4:5], off offset:16
	global_load_dwordx4 v[134:137], v[4:5], off offset:80
	global_load_dwordx4 v[130:133], v[4:5], off offset:64
	s_mul_i32 s8, s2, 0x30c000
	s_movk_i32 s2, 0xc00
	s_mul_hi_i32 s9, s3, 0x6000
	v_mul_lo_u32 v50, v6, s2
	s_add_u32 s20, s6, s8
	v_and_b32_e32 v3, 63, v52
	v_bfe_u32 v198, v52, 5, 1
	s_addc_u32 s21, s7, s9
	v_lshlrev_b32_e32 v4, 4, v7
	v_ashrrev_i32_e32 v51, 31, v50
	v_lshl_or_b32 v199, v198, 11, v4
	v_lshl_add_u64 v[4:5], s[20:21], 0, v[50:51]
	v_lshlrev_b32_e32 v178, 4, v3
	v_readfirstlane_b32 s60, v50
	v_lshl_add_u64 v[18:19], v[4:5], 0, v[178:179]
	s_mov_b64 s[20:21], 0x35800100
	s_add_i32 s60, s60, 0
	v_lshl_add_u64 v[4:5], v[18:19], 0, s[20:21]
	s_mov_b32 s2, m0
	s_mov_b32 m0, s60
	s_nop 0
	global_load_lds_dwordx4 v[4:5], off
	s_mov_b32 m0, s2
	s_mov_b64 s[20:21], 0x35800500
	v_lshl_add_u64 v[4:5], v[18:19], 0, s[20:21]
	s_add_i32 s2, s60, 0x400
	s_mov_b32 s3, m0
	s_mov_b32 m0, s2
	s_nop 0
	global_load_lds_dwordx4 v[4:5], off
	s_mov_b32 m0, s3
	s_mov_b64 s[20:21], 0x35800900
	v_lshl_add_u64 v[4:5], v[18:19], 0, s[20:21]
	s_add_i32 s2, s60, 0x800
	s_mov_b32 s3, m0
	s_mov_b32 m0, s2
	s_nop 0
	global_load_lds_dwordx4 v[4:5], off
	s_mov_b32 m0, s3
	s_waitcnt vmcnt(0)
	s_waitcnt lgkmcnt(0)
	s_barrier
; #define LAS __attribute__((address_space(3)))
; DEV float ex2(float x) { return __builtin_amdgcn_exp2f(x); }
; #define MFMA8(a, b, c) __builtin_amdgcn_mfma_scale_f32_32x32x64_f8f6f4((a), (b), (c), 0, 0, 0, 0x7f7f7f7f, 0, 0x7c7c7c7c)
; #define MLA_ISSUE(t_, st_) do { const unsigned char* s_ = imgs + (size_t)(t_) * MLA_IMG + wid * (STG / 8) + lane * 16; const unsigned d_ = ldsw + (unsigned)((st_) * STG); \
;     _Pragma("unroll") for (int i_ = 0; i_ < STG / 8192; ++i_) glds16a(s_ + i_ * 1024, d_ + i_ * 1024); } while (0)
; template <int VAR> DEV void mla_unit(const Params& p, int layer, int b, int hd, int tokbase, int t0, int t1, LAS char* lds, SideJob& sj) {
;     ...
;     if (ns > 1) MLA_ISSUE(t0 + 1, 1);
;     { LAS char* kp = lds + koffl;
;       sA0 = MFMA8(mla_kf8(kp, 0, 0), qf[0], cini); sA1 = MFMA8(mla_kf8(kp, 1, 0), qf[0], cini);
;       sA0 = MFMA8(mla_kf8(kp, 0, 1), qf[1], sA0); sA1 = MFMA8(mla_kf8(kp, 1, 1), qf[1], sA1);
; #pragma unroll
;       for (int i = 0; i < 16; ++i) { sA0[i] = ex2(sA0[i]); sA1[i] = ex2(sA1[i]); } }
;     int slot = 0;
;     v8i pw = {0, 0, 0, 0, 0, 0, 0, 0};
	s_mov_b64 s[20:21], 0x35806100
	v_lshl_add_u64 v[20:21], v[18:19], 0, s[20:21]
	s_add_i32 s2, s60, 0x6000
	s_mov_b32 s3, m0
	s_mov_b32 m0, s2
	s_nop 0
	global_load_lds_dwordx4 v[20:21], off
	s_mov_b32 m0, s3
	s_mov_b64 s[20:21], 0x35806500
	v_lshl_add_u64 v[20:21], v[18:19], 0, s[20:21]
	s_add_i32 s2, s60, 0x6400
	s_mov_b32 s3, m0
	s_mov_b32 m0, s2
	s_nop 0
	global_load_lds_dwordx4 v[20:21], off
	s_mov_b32 m0, s3
	s_mov_b64 s[20:21], 0x35806900
	v_lshl_add_u64 v[18:19], v[18:19], 0, s[20:21]
	s_add_i32 s2, s60, 0x6800
	s_mov_b32 s3, m0
	s_mov_b32 m0, s2
	s_nop 0
	global_load_lds_dwordx4 v[18:19], off
	s_mov_b32 m0, s3
	v_add_u32_e32 v200, 0, v199
	ds_read_b128 v[18:21], v200
	ds_read_b128 v[22:25], v200 offset:1024
	s_waitcnt vmcnt(3)
	v_ashrrev_i32_e32 v191, 4, v52
	s_movk_i32 s2, 0x104
	v_ashrrev_i32_e32 v195, 3, v52
	v_ashrrev_i32_e32 v181, 31, v180
	s_mov_b32 s62, 0
	v_mov_b32_e32 v193, v179
	v_mov_b32_e32 v146, 0
	v_mov_b32_e32 v147, 0
	v_mov_b32_e32 v148, 0
	v_mov_b32_e32 v149, 0
	v_mov_b32_e32 v150, 0
	v_mov_b32_e32 v151, 0
	v_mov_b32_e32 v152, 0
	v_mov_b32_e32 v153, 0
	s_mov_b32 s61, 0
	v_sub_f32_e32 v2, 0x41700000, v8
	v_mov_b32_e32 v3, v2
	v_mov_b32_e32 v4, v2
	v_mov_b32_e32 v5, v2
	v_mov_b32_e32 v6, v2
	v_mov_b32_e32 v7, v2
	v_mov_b32_e32 v8, v2
	v_mov_b32_e32 v9, v2
	v_mov_b32_e32 v10, v2
	v_mov_b32_e32 v11, v2
	v_mov_b32_e32 v12, v2
	v_mov_b32_e32 v13, v2
	v_mov_b32_e32 v14, v2
	v_mov_b32_e32 v15, v2
	v_mov_b32_e32 v16, v2
	v_mov_b32_e32 v17, v2
	s_waitcnt lgkmcnt(0)
	s_nop 0
	v_mfma_scale_f32_32x32x64_f8f6f4 v[18:33], v[18:25], v[138:145], v[2:17], v209, v208 op_sel_hi:[0,0,0]
	ds_read_b128 v[34:37], v200 offset:512
	ds_read_b128 v[38:41], v200 offset:1536
	s_waitcnt lgkmcnt(0)
	v_mfma_scale_f32_32x32x64_f8f6f4 v[34:49], v[34:41], v[138:145], v[2:17], v209, v208 op_sel_hi:[0,0,0]
	ds_read_b128 v[54:57], v200 offset:4096
	ds_read_b128 v[58:61], v200 offset:5120
	s_waitcnt lgkmcnt(0)
	v_mfma_scale_f32_32x32x64_f8f6f4 v[18:33], v[54:61], v[130:137], v[18:33], v209, v208 op_sel_hi:[0,0,0]
	ds_read_b128 v[54:57], v200 offset:4608
	ds_read_b128 v[58:61], v200 offset:5632
	s_waitcnt lgkmcnt(0)
	v_mfma_scale_f32_32x32x64_f8f6f4 v[34:49], v[54:61], v[130:137], v[34:49], v209, v208 op_sel_hi:[0,0,0]
	s_nop 15
	v_exp_f32_e32 v82, v18
	v_lshlrev_b32_e32 v18, 2, v52
	v_and_b32_e32 v190, 60, v18
	v_exp_f32_e32 v83, v19
	v_mul_lo_u32 v18, v191, s2
	s_add_i32 s2, 0, 0x12000
	v_lshlrev_b32_e32 v19, 2, v190
	v_add3_u32 v194, s2, v18, v19
	v_lshlrev_b32_e32 v18, 3, v52
	v_exp_f32_e32 v84, v20
	v_exp_f32_e32 v85, v21
	v_exp_f32_e32 v86, v22
	v_exp_f32_e32 v87, v23
	v_exp_f32_e32 v88, v24
	v_exp_f32_e32 v89, v25
	v_exp_f32_e32 v66, v34
	v_exp_f32_e32 v67, v35
	v_exp_f32_e32 v68, v36
	v_mov_b32_e32 v69, v37
	v_mov_b32_e32 v70, v38
	v_mov_b32_e32 v71, v39
	v_mov_b32_e32 v72, v40
	v_mov_b32_e32 v73, v41
	v_mov_b32_e32 v74, v42
	v_mov_b32_e32 v75, v43
	v_mov_b32_e32 v76, v44
	v_mov_b32_e32 v77, v45
	v_mov_b32_e32 v78, v46
	v_mov_b32_e32 v79, v47
	v_mov_b32_e32 v80, v48
	v_mov_b32_e32 v81, v49
	v_exp_f32_e32 v90, v26
	v_exp_f32_e32 v91, v27
	v_exp_f32_e32 v92, v28
	v_exp_f32_e32 v93, v29
	v_exp_f32_e32 v94, v30
	v_exp_f32_e32 v95, v31
	v_exp_f32_e32 v96, v32
	v_exp_f32_e32 v97, v33
	v_and_b32_e32 v192, 56, v18
	v_or_b32_e32 v18, s8, v178
	v_mov_b32_e32 v19, s9
	v_lshl_add_u64 v[18:19], v[18:19], 0, v[50:51]
	v_lshl_add_u64 v[18:19], s[6:7], 0, v[18:19]
	s_mov_b64 s[8:9], 0x3580c100
	v_mov_b32_e32 v34, 0
	v_cmp_lt_u32_e64 s[40:41], 31, v190
	v_lshl_add_u32 v196, v195, 2, s2
	v_mul_u32_u24_e32 v197, 0x104, v192
	v_lshl_add_u64 v[162:163], v[18:19], 0, s[8:9]
	v_mov_b32_e32 v35, v34
	v_mov_b32_e32 v36, v34
	v_mov_b32_e32 v37, v34
	v_mov_b32_e32 v38, v34
	v_mov_b32_e32 v39, v34
	v_mov_b32_e32 v40, v34
	v_mov_b32_e32 v41, v34
	v_mov_b32_e32 v42, v34
	v_mov_b32_e32 v43, v34
	v_mov_b32_e32 v44, v34
	v_mov_b32_e32 v45, v34
	v_mov_b32_e32 v46, v34
	v_mov_b32_e32 v47, v34
	v_mov_b32_e32 v48, v34
	v_mov_b32_e32 v49, v34
	v_mov_b32_e32 v18, v34
	v_mov_b32_e32 v19, v34
	v_mov_b32_e32 v20, v34
	v_mov_b32_e32 v21, v34
	v_mov_b32_e32 v22, v34
	v_mov_b32_e32 v23, v34
	v_mov_b32_e32 v24, v34
	v_mov_b32_e32 v25, v34
	v_mov_b32_e32 v26, v34
	v_mov_b32_e32 v27, v34
	v_mov_b32_e32 v28, v34
	v_mov_b32_e32 v29, v34
	v_mov_b32_e32 v30, v34
	v_mov_b32_e32 v31, v34
	v_mov_b32_e32 v32, v34
	v_mov_b32_e32 v33, v34
	v_mov_b32_e32 v50, v34
	v_mov_b32_e32 v51, v34
	v_mov_b32_e32 v52, v34
	v_mov_b32_e32 v53, v34
	v_mov_b32_e32 v54, v34
	v_mov_b32_e32 v55, v34
	v_mov_b32_e32 v56, v34
	v_mov_b32_e32 v57, v34
	v_mov_b32_e32 v58, v34
	v_mov_b32_e32 v59, v34
	v_mov_b32_e32 v60, v34
	v_mov_b32_e32 v61, v34
	v_mov_b32_e32 v62, v34
	v_mov_b32_e32 v63, v34
	v_mov_b32_e32 v64, v34
	v_mov_b32_e32 v65, v34
	v_mov_b64_e32 v[210:211], s[76:77]
	v_mov_b64_e32 v[212:213], s[78:79]
	v_mov_b64_e32 v[214:215], s[80:81]
	v_mov_b64_e32 v[216:217], s[82:83]
	s_branch .LBB0_813
